# speedup vs baseline: 1.0058x; 1.0058x over previous
.LBB0_22:
	s_or_b64 exec, exec, s[0:1]
	v_lshlrev_b64 v[20:21], 5, v[26:27]
	v_lshl_add_u64 v[20:21], v[28:29], 0, v[20:21]
	global_load_dwordx4 v[32:35], v[20:21], off nt
	global_load_dwordx4 v[36:39], v[20:21], off offset:16 nt
	s_waitcnt vmcnt(4)
	v_cvt_pk_f16_f32 v4, v4, v5
	v_cvt_pk_f16_f32 v5, v6, v7
	v_cvt_pk_f16_f32 v6, v0, v1
	v_cvt_pk_f16_f32 v7, v2, v3
	v_lshl_add_u64 v[16:17], v[16:17], 4, v[18:19]
	s_waitcnt vmcnt(2)
	v_cvt_pk_f16_f32 v0, v12, v13
	v_cvt_pk_f16_f32 v1, v14, v15
	v_cvt_pk_f16_f32 v2, v8, v9
	v_cvt_pk_f16_f32 v3, v10, v11
	v_lshl_add_u64 v[8:9], v[22:23], 4, v[24:25]
	global_store_dwordx4 v[16:17], v[4:7], off sc0 sc1
	global_store_dwordx4 v[8:9], v[0:3], off sc0 sc1
	s_nop 0
	v_lshl_add_u64 v[4:5], v[26:27], 4, v[30:31]
	s_waitcnt vmcnt(3)
	v_cvt_pk_f16_f32 v0, v32, v33
	v_cvt_pk_f16_f32 v1, v34, v35
	s_waitcnt vmcnt(2)
	v_cvt_pk_f16_f32 v2, v36, v37
	v_cvt_pk_f16_f32 v3, v38, v39
	global_store_dwordx4 v[4:5], v[0:3], off sc0 sc1
	s_endpgm

.Lmsk_8416:
	s_and_saveexec_b64 s[2:3], s[0:1]
	v_add_f32_e32 v34, v51, v34
	ds_write_b32 v223, v34 offset:49280
	s_or_b64 exec, exec, s[2:3]
	s_waitcnt lgkmcnt(0)
	ds_read_b128 v[34:37], v50 offset:49280
	ds_read_b128 v[38:41], v50 offset:49312
	s_lshl_b64 s[2:3], s[14:15], 1
	s_add_u32 s2, s10, s2
	s_addc_u32 s3, s11, s3
	s_waitcnt lgkmcnt(1)
	v_rcp_f32_e32 v42, v34
	v_rcp_f32_e32 v43, v35
	s_lshl_b32 s6, s34, 12
	s_add_i32 s6, s6, 0
	v_lshlrev_b32_e32 v230, 1, v222
	v_lshlrev_b32_e32 v231, 9, v211
	v_rcp_f32_e32 v44, v36
	v_rcp_f32_e32 v45, v37
	s_waitcnt lgkmcnt(0)
	v_rcp_f32_e32 v46, v38
	ds_read_b128 v[34:37], v50 offset:49344
	v_rcp_f32_e32 v47, v39
	v_rcp_f32_e32 v48, v40
	v_rcp_f32_e32 v49, v41
	ds_read_b128 v[38:41], v50 offset:49376
	v_add3_u32 v50, s6, v230, v231
	v_fma_mixlo_f16 v2, v2, v42, 0
	ds_write_b16 v50, v2 offset:51200
	v_fma_mixlo_f16 v2, v18, v42, 0
	ds_write_b16 v50, v2 offset:51264
	v_fma_mixlo_f16 v2, v3, v43, 0
	ds_write_b16 v50, v2 offset:51328
	v_fma_mixlo_f16 v2, v19, v43, 0
	ds_write_b16 v50, v2 offset:51392
	v_fma_mixlo_f16 v2, v4, v44, 0
	ds_write_b16 v50, v2 offset:51456
	v_fma_mixlo_f16 v2, v20, v44, 0
	ds_write_b16 v50, v2 offset:51520
	v_fma_mixlo_f16 v2, v5, v45, 0
	ds_write_b16 v50, v2 offset:51584
	v_fma_mixlo_f16 v2, v21, v45, 0
	ds_write_b16 v50, v2 offset:51648
	v_fma_mixlo_f16 v2, v6, v46, 0
	ds_write_b16 v50, v2 offset:52224
	v_fma_mixlo_f16 v2, v22, v46, 0
	ds_write_b16 v50, v2 offset:52288
	v_fma_mixlo_f16 v2, v7, v47, 0
	ds_write_b16 v50, v2 offset:52352
	v_fma_mixlo_f16 v2, v23, v47, 0
	s_waitcnt lgkmcnt(12)
	v_rcp_f32_e32 v34, v34
	ds_write_b16 v50, v2 offset:52416
	v_fma_mixlo_f16 v2, v8, v48, 0
	ds_write_b16 v50, v2 offset:52480
	v_fma_mixlo_f16 v2, v24, v48, 0
	v_rcp_f32_e32 v35, v35
	ds_write_b16 v50, v2 offset:52544
	v_fma_mixlo_f16 v2, v9, v49, 0
	ds_write_b16 v50, v2 offset:52608
	v_fma_mixlo_f16 v2, v25, v49, 0
	v_rcp_f32_e32 v36, v36
	ds_write_b16 v50, v2 offset:52672
	v_fma_mixlo_f16 v2, v10, v34, 0
	ds_write_b16 v50, v2 offset:53248
	v_fma_mixlo_f16 v2, v26, v34, 0
	v_rcp_f32_e32 v37, v37
	ds_write_b16 v50, v2 offset:53312
	v_fma_mixlo_f16 v2, v11, v35, 0
	ds_write_b16 v50, v2 offset:53376
	v_fma_mixlo_f16 v2, v27, v35, 0
	s_waitcnt lgkmcnt(14)
	v_rcp_f32_e32 v38, v38
	ds_write_b16 v50, v2 offset:53440
	v_fma_mixlo_f16 v2, v12, v36, 0
	ds_write_b16 v50, v2 offset:53504
	v_fma_mixlo_f16 v2, v28, v36, 0
	v_rcp_f32_e32 v39, v39
	ds_write_b16 v50, v2 offset:53568
	v_fma_mixlo_f16 v2, v13, v37, 0
	ds_write_b16 v50, v2 offset:53632
	v_fma_mixlo_f16 v2, v29, v37, 0
	v_rcp_f32_e32 v40, v40
	ds_write_b16 v50, v2 offset:53696
	v_fma_mixlo_f16 v2, v14, v38, 0
	ds_write_b16 v50, v2 offset:54272
	v_fma_mixlo_f16 v2, v30, v38, 0
	v_rcp_f32_e32 v41, v41
	ds_write_b16 v50, v2 offset:54336
	v_fma_mixlo_f16 v2, v15, v39, 0
	ds_write_b16 v50, v2 offset:54400
	v_fma_mixlo_f16 v2, v31, v39, 0
	ds_write_b16 v50, v2 offset:54464
	v_fma_mixlo_f16 v2, v16, v40, 0
	ds_write_b16 v50, v2 offset:54528
	v_fma_mixlo_f16 v2, v32, v40, 0
	ds_write_b16 v50, v2 offset:54592
	v_fma_mixlo_f16 v2, v17, v41, 0
	ds_write_b16 v50, v2 offset:54656
	v_fma_mixlo_f16 v2, v33, v41, 0
	ds_write_b16 v50, v2 offset:54720
	v_and_b32_e32 v2, 56, v209
	s_lshl_b32 s22, s33, 1
	v_lshrrev_b32_e32 v36, 3, v207
	v_lshlrev_b32_e32 v220, 1, v2
	s_add_u32 s2, s2, s22
	v_add_u32_e32 v14, s6, v220
	v_lshlrev_b32_e32 v232, 7, v36
	s_addc_u32 s3, s3, 0
	s_waitcnt lgkmcnt(0)
	v_mov_b32_e32 v221, 0
	v_add_u32_e32 v2, v14, v232
	v_or_b32_e32 v37, 8, v36
	v_lshl_add_u64 v[10:11], s[2:3], 0, v[220:221]
	ds_read_b128 v[2:5], v2 offset:51200
	v_lshlrev_b32_e32 v6, 11, v36
	v_mov_b32_e32 v7, v221
	v_lshlrev_b32_e32 v233, 7, v37
	v_readfirstlane_b32 s8, v0
	v_lshl_add_u64 v[12:13], v[10:11], 0, v[6:7]
	v_add_u32_e32 v6, v14, v233
	s_lshr_b32 s23, s8, 6
	ds_read_b128 v[6:9], v6 offset:51200
	s_or_b32 s2, s12, s27
	s_lshl_b32 s12, s23, 5
	s_add_u32 s6, s2, s12
	s_addc_u32 s7, s13, 0
	s_waitcnt lgkmcnt(1)
	global_store_dwordx4 v[12:13], v[2:5], off sc0 sc1
	v_or_b32_e32 v38, 16, v36
	s_lshl_b64 s[2:3], s[6:7], 11
	v_lshlrev_b32_e32 v2, 11, v37
	v_mov_b32_e32 v3, v221
	v_lshl_add_u64 v[2:3], v[10:11], 0, v[2:3]
	v_lshlrev_b32_e32 v234, 7, v38
	s_add_u32 s2, s4, s2
	s_waitcnt lgkmcnt(0)
	global_store_dwordx4 v[2:3], v[6:9], off sc0 sc1
	v_add_u32_e32 v2, v14, v234
	v_or_b32_e32 v39, 24, v36
	s_addc_u32 s3, s5, s3
	ds_read_b128 v[2:5], v2 offset:51200
	v_lshlrev_b32_e32 v6, 11, v38
	v_mov_b32_e32 v7, v221
	v_lshlrev_b32_e32 v235, 7, v39
	s_add_u32 s2, s2, s22
	v_lshl_add_u64 v[12:13], v[10:11], 0, v[6:7]
	v_add_u32_e32 v6, v14, v235
	s_addc_u32 s3, s3, 0
	s_lshl_b32 s4, s8, 4
	ds_read_b128 v[6:9], v6 offset:51200
	s_and_b32 s4, s4, 0xfffff000
	s_add_u32 s4, s30, s4
	s_addc_u32 s5, s31, 0
	s_lshr_b32 s9, s8, 2
	s_waitcnt lgkmcnt(1)
	global_store_dwordx4 v[12:13], v[2:5], off sc0 sc1
	v_and_or_b32 v0, s9, 48, v1
	s_lshl_b32 s9, s23, 10
	v_lshlrev_b32_e32 v2, 11, v39
	v_mov_b32_e32 v3, v221
	v_lshl_add_u64 v[2:3], v[10:11], 0, v[2:3]
	v_lshlrev_b32_e32 v0, 6, v0
	v_mov_b32_e32 v1, v221
	s_cmp_lg_u32 0, -1
	s_waitcnt lgkmcnt(0)
	global_store_dwordx4 v[2:3], v[6:9], off sc0 sc1
	v_lshl_add_u64 v[0:1], s[4:5], 0, v[0:1]
	s_cselect_b32 s4, 0, 0
	s_waitcnt lgkmcnt(0)
	s_barrier
	v_lshlrev_b32_e32 v2, 1, v208
	v_mov_b32_e32 v3, v221
	s_add_i32 s25, s4, s9
	v_lshl_add_u64 v[208:209], v[0:1], 0, v[2:3]
	s_addk_i32 s25, 0x6000
	s_mov_b32 s4, m0
	s_mov_b32 m0, s25
	s_nop 0
	global_load_lds_dwordx4 v[208:209], off
	s_mov_b32 m0, s4
	v_lshlrev_b32_e32 v0, 1, v210
	v_mov_b32_e32 v0, v221
	v_mov_b32_e32 v1, v221
	v_mov_b32_e32 v2, v221
	v_mov_b32_e32 v4, v221
	v_mov_b32_e32 v5, v221
	v_mov_b32_e32 v6, v221
	v_mov_b32_e32 v7, v221
	v_mov_b32_e32 v8, v221
	v_mov_b32_e32 v9, v221
	v_mov_b32_e32 v10, v221
	v_mov_b32_e32 v11, v221
	v_mov_b32_e32 v12, v221
	v_mov_b32_e32 v13, v221
	v_mov_b32_e32 v14, v221
	v_mov_b32_e32 v15, v221
	s_waitcnt vmcnt(5) lgkmcnt(0)
	s_barrier
	ds_read_b128 v[32:35], v224
	s_cmp_lg_u32 s26, 0
	s_waitcnt lgkmcnt(0)
	v_mfma_f32_32x32x16_f16 v[16:31], v[32:35], v[156:159], v[0:15]
	ds_read_b128 v[32:35], v224 offset:512
	s_cselect_b64 s[2:3], -1, 0
	v_lshlrev_b32_e32 v239, 10, v36
	v_lshlrev_b32_e32 v238, 10, v37
	v_lshlrev_b32_e32 v237, 10, v38
	v_lshlrev_b32_e32 v236, 10, v39
	v_or_b32_e32 v221, s12, v222
	s_waitcnt lgkmcnt(0)
	v_mfma_f32_32x32x16_f16 v[0:15], v[32:35], v[156:159], v[0:15]
	ds_read_b128 v[32:35], v224 offset:2048
	s_and_b64 vcc, exec, s[2:3]
	s_waitcnt lgkmcnt(0)
	v_mfma_f32_32x32x16_f16 v[16:31], v[32:35], v[152:155], v[16:31]
	ds_read_b128 v[32:35], v224 offset:2560
	s_waitcnt lgkmcnt(0)
	v_mfma_f32_32x32x16_f16 v[0:15], v[32:35], v[152:155], v[0:15]
	ds_read_b128 v[32:35], v224 offset:4096
	s_waitcnt lgkmcnt(0)
	v_mfma_f32_32x32x16_f16 v[16:31], v[32:35], v[148:151], v[16:31]
	ds_read_b128 v[32:35], v224 offset:4608
	s_waitcnt lgkmcnt(0)
	v_mfma_f32_32x32x16_f16 v[0:15], v[32:35], v[148:151], v[0:15]
	ds_read_b128 v[32:35], v224 offset:6144
	s_waitcnt lgkmcnt(0)
	v_mfma_f32_32x32x16_f16 v[16:31], v[32:35], v[144:147], v[16:31]
	ds_read_b128 v[32:35], v224 offset:6656
	s_waitcnt lgkmcnt(0)
	v_mfma_f32_32x32x16_f16 v[0:15], v[32:35], v[144:147], v[0:15]
	s_nop 15
	s_nop 7
	s_cbranch_vccnz .LBB2_119
	v_readfirstlane_b32 s12, v221
	s_cmp_lt_i32 s12, 0
	s_cbranch_scc1 .LBB2_111
	s_cmp_gt_u32 s12, 31
	s_cbranch_scc1 .LBB2_112
	v_mov_b32_e32 v32, 0xff800000
	v_cmp_lt_u32_e32 vcc, v227, v221
	v_or_b32_e32 v33, 2, v227
	s_mov_b32 s13, 0xff800000
	v_cndmask_b32_e32 v17, v32, v17, vcc
	v_cmp_le_u32_e32 vcc, v227, v221
	s_nop 1
	v_cndmask_b32_e32 v16, v32, v16, vcc
	v_cmp_le_u32_e32 vcc, v33, v221
	v_or_b32_e32 v33, 3, v227
	s_nop 0
	v_cndmask_b32_e32 v18, v32, v18, vcc
	v_cmp_le_u32_e32 vcc, v33, v221
	v_or_b32_e32 v33, 8, v227
	s_nop 0
	v_cndmask_b32_e32 v19, v32, v19, vcc
	v_cmp_le_u32_e32 vcc, v33, v221
	v_or_b32_e32 v33, 9, v227
	s_nop 0
	v_cndmask_b32_e32 v20, v32, v20, vcc
	v_cmp_le_u32_e32 vcc, v33, v221
	v_or_b32_e32 v33, 10, v227
	s_nop 0
	v_cndmask_b32_e32 v21, v32, v21, vcc
	v_cmp_le_u32_e32 vcc, v33, v221
	v_or_b32_e32 v33, 11, v227
	s_nop 0
	v_cndmask_b32_e32 v22, v32, v22, vcc
	v_cmp_le_u32_e32 vcc, v33, v221
	v_or_b32_e32 v33, 16, v227
	s_nop 0
	v_cndmask_b32_e32 v23, v32, v23, vcc
	v_cmp_le_u32_e32 vcc, v33, v221
	v_or_b32_e32 v33, 17, v227
	s_nop 0
	v_cndmask_b32_e32 v24, v32, v24, vcc
	v_cmp_le_u32_e32 vcc, v33, v221
	v_or_b32_e32 v33, 18, v227
	s_nop 0
	v_cndmask_b32_e32 v25, v32, v25, vcc
	v_cmp_le_u32_e32 vcc, v33, v221
	v_or_b32_e32 v33, 19, v227
	s_nop 0
	v_cndmask_b32_e32 v26, v32, v26, vcc
	v_cmp_le_u32_e32 vcc, v33, v221
	v_or_b32_e32 v33, 24, v227
	s_nop 0
	v_cndmask_b32_e32 v27, v32, v27, vcc
	v_cmp_le_u32_e32 vcc, v33, v221
	v_or_b32_e32 v33, 25, v227
	s_nop 0
	v_cndmask_b32_e32 v28, v32, v28, vcc
	v_cmp_le_u32_e32 vcc, v33, v221
	v_or_b32_e32 v33, 26, v227
	s_nop 0
	v_cndmask_b32_e32 v29, v32, v29, vcc
	v_cmp_le_u32_e32 vcc, v33, v221
	s_nop 1
	v_cndmask_b32_e32 v30, v32, v30, vcc
	v_or_b32_e32 v32, 27, v227
	v_cmp_gt_u32_e32 vcc, v32, v221
	s_and_saveexec_b64 s[4:5], vcc
	v_mov_b32_e32 v31, s13
	s_or_b64 exec, exec, s[4:5]
	s_branch .LBB2_112

.Lmsk_11826:
	s_and_saveexec_b64 s[2:3], s[0:1]
	v_add_f32_e32 v32, v49, v32
	ds_write_b32 v240, v32 offset:49280
	s_or_b64 exec, exec, s[2:3]
	s_waitcnt lgkmcnt(0)
	ds_read_b128 v[32:35], v48 offset:49280
	ds_read_b128 v[36:39], v48 offset:49312
	s_lshl_b64 s[0:1], s[4:5], 1
	s_add_u32 s0, s10, s0
	s_addc_u32 s1, s11, s1
	s_waitcnt lgkmcnt(1)
	v_rcp_f32_e32 v40, v32
	v_rcp_f32_e32 v41, v33
	s_lshl_b32 s2, s23, 12
	s_add_i32 s2, s2, 0
	v_rcp_f32_e32 v42, v34
	v_rcp_f32_e32 v43, v35
	s_waitcnt lgkmcnt(0)
	v_rcp_f32_e32 v44, v36
	ds_read_b128 v[32:35], v48 offset:49344
	v_rcp_f32_e32 v45, v37
	v_rcp_f32_e32 v46, v38
	v_rcp_f32_e32 v47, v39
	ds_read_b128 v[36:39], v48 offset:49376
	v_add3_u32 v48, s2, v230, v231
	v_fma_mixlo_f16 v0, v0, v40, 0
	ds_write_b16 v48, v0 offset:51200
	v_fma_mixlo_f16 v0, v16, v40, 0
	ds_write_b16 v48, v0 offset:51264
	v_fma_mixlo_f16 v0, v1, v41, 0
	ds_write_b16 v48, v0 offset:51328
	v_fma_mixlo_f16 v0, v17, v41, 0
	ds_write_b16 v48, v0 offset:51392
	v_fma_mixlo_f16 v0, v2, v42, 0
	ds_write_b16 v48, v0 offset:51456
	v_fma_mixlo_f16 v0, v18, v42, 0
	ds_write_b16 v48, v0 offset:51520
	v_fma_mixlo_f16 v0, v3, v43, 0
	ds_write_b16 v48, v0 offset:51584
	v_fma_mixlo_f16 v0, v19, v43, 0
	ds_write_b16 v48, v0 offset:51648
	v_fma_mixlo_f16 v0, v4, v44, 0
	ds_write_b16 v48, v0 offset:52224
	v_fma_mixlo_f16 v0, v20, v44, 0
	ds_write_b16 v48, v0 offset:52288
	v_fma_mixlo_f16 v0, v5, v45, 0
	ds_write_b16 v48, v0 offset:52352
	v_fma_mixlo_f16 v0, v21, v45, 0
	s_waitcnt lgkmcnt(12)
	v_rcp_f32_e32 v32, v32
	ds_write_b16 v48, v0 offset:52416
	v_fma_mixlo_f16 v0, v6, v46, 0
	ds_write_b16 v48, v0 offset:52480
	v_fma_mixlo_f16 v0, v22, v46, 0
	v_rcp_f32_e32 v33, v33
	ds_write_b16 v48, v0 offset:52544
	v_fma_mixlo_f16 v0, v7, v47, 0
	ds_write_b16 v48, v0 offset:52608
	v_fma_mixlo_f16 v0, v23, v47, 0
	v_rcp_f32_e32 v34, v34
	ds_write_b16 v48, v0 offset:52672
	v_fma_mixlo_f16 v0, v8, v32, 0
	ds_write_b16 v48, v0 offset:53248
	v_fma_mixlo_f16 v0, v24, v32, 0
	v_rcp_f32_e32 v35, v35
	ds_write_b16 v48, v0 offset:53312
	v_fma_mixlo_f16 v0, v9, v33, 0
	ds_write_b16 v48, v0 offset:53376
	v_fma_mixlo_f16 v0, v25, v33, 0
	s_waitcnt lgkmcnt(14)
	v_rcp_f32_e32 v36, v36
	ds_write_b16 v48, v0 offset:53440
	v_fma_mixlo_f16 v0, v10, v34, 0
	ds_write_b16 v48, v0 offset:53504
	v_fma_mixlo_f16 v0, v26, v34, 0
	v_rcp_f32_e32 v37, v37
	ds_write_b16 v48, v0 offset:53568
	v_fma_mixlo_f16 v0, v11, v35, 0
	ds_write_b16 v48, v0 offset:53632
	v_fma_mixlo_f16 v0, v27, v35, 0
	v_rcp_f32_e32 v38, v38
	ds_write_b16 v48, v0 offset:53696
	v_fma_mixlo_f16 v0, v12, v36, 0
	ds_write_b16 v48, v0 offset:54272
	v_fma_mixlo_f16 v0, v28, v36, 0
	v_rcp_f32_e32 v39, v39
	ds_write_b16 v48, v0 offset:54336
	v_fma_mixlo_f16 v0, v13, v37, 0
	ds_write_b16 v48, v0 offset:54400
	v_fma_mixlo_f16 v0, v29, v37, 0
	ds_write_b16 v48, v0 offset:54464
	v_fma_mixlo_f16 v0, v14, v38, 0
	ds_write_b16 v48, v0 offset:54528
	v_fma_mixlo_f16 v0, v30, v38, 0
	ds_write_b16 v48, v0 offset:54592
	v_fma_mixlo_f16 v0, v15, v39, 0
	ds_write_b16 v48, v0 offset:54656
	v_fma_mixlo_f16 v0, v31, v39, 0
	ds_write_b16 v48, v0 offset:54720
	v_add_u32_e32 v12, s2, v220
	s_waitcnt lgkmcnt(0)
	v_add_u32_e32 v0, v12, v232
	ds_read_b128 v[0:3], v0 offset:51200
	v_add_u32_e32 v4, v12, v233
	s_add_u32 s0, s0, s22
	ds_read_b128 v[4:7], v4 offset:51200
	s_addc_u32 s1, s1, 0
	v_mov_b32_e32 v221, 0
	v_lshl_add_u64 v[8:9], s[0:1], 0, v[220:221]
	v_lshlrev_b32_e32 v220, 1, v239
	v_lshl_add_u64 v[10:11], v[8:9], 0, v[220:221]
	v_lshlrev_b32_e32 v220, 1, v238
	s_waitcnt lgkmcnt(1)
	global_store_dwordx4 v[10:11], v[0:3], off sc0 sc1
	s_nop 1
	v_lshl_add_u64 v[0:1], v[8:9], 0, v[220:221]
	s_waitcnt lgkmcnt(0)
	global_store_dwordx4 v[0:1], v[4:7], off sc0 sc1
	v_add_u32_e32 v0, v12, v234
	ds_read_b128 v[0:3], v0 offset:51200
	v_add_u32_e32 v4, v12, v235
	ds_read_b128 v[4:7], v4 offset:51200
	v_lshlrev_b32_e32 v220, 1, v237
	v_lshl_add_u64 v[10:11], v[8:9], 0, v[220:221]
	v_lshlrev_b32_e32 v220, 1, v236
	s_waitcnt lgkmcnt(1)
	global_store_dwordx4 v[10:11], v[0:3], off sc0 sc1
	s_nop 1
	v_lshl_add_u64 v[0:1], v[8:9], 0, v[220:221]
	s_waitcnt lgkmcnt(0)
	global_store_dwordx4 v[0:1], v[4:7], off sc0 sc1
	s_waitcnt lgkmcnt(0)
	s_barrier
	s_endpgm
